# non-temporal hint on converted-weight stores in both converter instances (P1 converter workgroups and P4 tail)
# speedup vs baseline: 1.0090x; 1.0012x over previous
; __device__ __forceinline__ void convert_item(Frame& F, int i0, LAS unsigned char* cvbuf) {
;     { const CvItem c = cv_decode(F, i0);
;         float x[128];
; #pragma unroll
;         for (int i = 0; i < 128; ++i) x[i] = c.src[(size_t)i * c.N];
.LBB0_258:
	s_lshl_b64 s[20:21], s[20:21], 2
	s_waitcnt vmcnt(62)
	global_load_dword v15, v[12:13], off
	v_lshl_add_u64 v[12:13], v[12:13], 0, s[20:21]
	v_lshl_add_u64 v[16:17], v[12:13], 0, s[20:21]
	v_lshl_add_u64 v[18:19], v[16:17], 0, s[20:21]
	v_lshl_add_u64 v[20:21], v[18:19], 0, s[20:21]
	v_lshl_add_u64 v[22:23], v[20:21], 0, s[20:21]
	v_lshl_add_u64 v[24:25], v[22:23], 0, s[20:21]
	v_lshl_add_u64 v[26:27], v[24:25], 0, s[20:21]
	v_lshl_add_u64 v[28:29], v[26:27], 0, s[20:21]
	global_load_dword v13, v[12:13], off
	s_nop 0
	global_load_dword v16, v[16:17], off
	s_nop 0
	global_load_dword v17, v[18:19], off
	s_nop 0
	global_load_dword v18, v[20:21], off
	global_load_dword v19, v[22:23], off
	s_nop 0
	global_load_dword v20, v[24:25], off
	global_load_dword v23, v[26:27], off
	global_load_dword v12, v[28:29], off
	v_lshl_add_u64 v[24:25], v[28:29], 0, s[20:21]
	v_lshl_add_u64 v[26:27], v[24:25], 0, s[20:21]
	global_load_dword v21, v[24:25], off
	global_load_dword v22, v[26:27], off
	v_lshl_add_u64 v[26:27], v[26:27], 0, s[20:21]
	global_load_dword v24, v[26:27], off
	v_lshl_add_u64 v[26:27], v[26:27], 0, s[20:21]
	v_lshl_add_u64 v[28:29], v[26:27], 0, s[20:21]
	v_lshl_add_u64 v[30:31], v[28:29], 0, s[20:21]
	v_lshl_add_u64 v[32:33], v[30:31], 0, s[20:21]
	global_load_dword v25, v[26:27], off
	s_andn2_b64 vcc, exec, s[18:19]
	global_load_dword v27, v[28:29], off
	s_mov_b64 s[18:19], -1
	global_load_dword v28, v[30:31], off
	s_nop 0
	global_load_dword v31, v[32:33], off
	v_lshl_add_u64 v[32:33], v[32:33], 0, s[20:21]
	global_load_dword v26, v[32:33], off
	v_lshl_add_u64 v[32:33], v[32:33], 0, s[20:21]
	global_load_dword v29, v[32:33], off
	v_lshl_add_u64 v[32:33], v[32:33], 0, s[20:21]
	v_lshl_add_u64 v[34:35], v[32:33], 0, s[20:21]
	global_load_dword v30, v[32:33], off
	s_nop 0
	global_load_dword v32, v[34:35], off
	v_lshl_add_u64 v[34:35], v[34:35], 0, s[20:21]
	v_lshl_add_u64 v[36:37], v[34:35], 0, s[20:21]
	v_lshl_add_u64 v[38:39], v[36:37], 0, s[20:21]
	v_lshl_add_u64 v[40:41], v[38:39], 0, s[20:21]
	global_load_dword v33, v[34:35], off
	s_nop 0
	global_load_dword v35, v[36:37], off
	s_nop 0
	global_load_dword v36, v[38:39], off
	s_nop 0
	global_load_dword v39, v[40:41], off
	v_lshl_add_u64 v[40:41], v[40:41], 0, s[20:21]
	global_load_dword v34, v[40:41], off
	v_lshl_add_u64 v[40:41], v[40:41], 0, s[20:21]
	global_load_dword v37, v[40:41], off
	v_lshl_add_u64 v[40:41], v[40:41], 0, s[20:21]
	v_lshl_add_u64 v[42:43], v[40:41], 0, s[20:21]
	global_load_dword v38, v[40:41], off
	s_nop 0
	global_load_dword v40, v[42:43], off
	v_lshl_add_u64 v[42:43], v[42:43], 0, s[20:21]
	v_lshl_add_u64 v[44:45], v[42:43], 0, s[20:21]
	v_lshl_add_u64 v[46:47], v[44:45], 0, s[20:21]
	v_lshl_add_u64 v[48:49], v[46:47], 0, s[20:21]
	global_load_dword v41, v[42:43], off
	s_nop 0
	global_load_dword v43, v[44:45], off
	s_nop 0
	global_load_dword v44, v[46:47], off
	s_nop 0
	global_load_dword v47, v[48:49], off
	v_lshl_add_u64 v[48:49], v[48:49], 0, s[20:21]
	global_load_dword v42, v[48:49], off
	v_lshl_add_u64 v[48:49], v[48:49], 0, s[20:21]
	global_load_dword v45, v[48:49], off
	v_lshl_add_u64 v[48:49], v[48:49], 0, s[20:21]
	v_lshl_add_u64 v[50:51], v[48:49], 0, s[20:21]
	global_load_dword v46, v[48:49], off
	s_nop 0
	global_load_dword v48, v[50:51], off
	v_lshl_add_u64 v[50:51], v[50:51], 0, s[20:21]
	v_lshl_add_u64 v[52:53], v[50:51], 0, s[20:21]
	v_lshl_add_u64 v[54:55], v[52:53], 0, s[20:21]
	v_lshl_add_u64 v[56:57], v[54:55], 0, s[20:21]
	global_load_dword v49, v[50:51], off
	s_nop 0
	global_load_dword v51, v[52:53], off
	s_nop 0
	global_load_dword v52, v[54:55], off
	s_nop 0
	global_load_dword v55, v[56:57], off
	v_lshl_add_u64 v[56:57], v[56:57], 0, s[20:21]
	global_load_dword v50, v[56:57], off
	v_lshl_add_u64 v[56:57], v[56:57], 0, s[20:21]
	global_load_dword v53, v[56:57], off
	v_lshl_add_u64 v[56:57], v[56:57], 0, s[20:21]
	v_lshl_add_u64 v[58:59], v[56:57], 0, s[20:21]
	global_load_dword v54, v[56:57], off
	s_nop 0
	global_load_dword v56, v[58:59], off
	v_lshl_add_u64 v[58:59], v[58:59], 0, s[20:21]
	v_lshl_add_u64 v[60:61], v[58:59], 0, s[20:21]
	v_lshl_add_u64 v[62:63], v[60:61], 0, s[20:21]
	v_lshl_add_u64 v[64:65], v[62:63], 0, s[20:21]
	global_load_dword v57, v[58:59], off
	s_nop 0
	global_load_dword v59, v[60:61], off
	s_nop 0
	global_load_dword v60, v[62:63], off
	s_nop 0
	global_load_dword v63, v[64:65], off
	v_lshl_add_u64 v[64:65], v[64:65], 0, s[20:21]
	global_load_dword v58, v[64:65], off
	v_lshl_add_u64 v[64:65], v[64:65], 0, s[20:21]
	global_load_dword v61, v[64:65], off
	v_lshl_add_u64 v[64:65], v[64:65], 0, s[20:21]
	v_lshl_add_u64 v[66:67], v[64:65], 0, s[20:21]
	global_load_dword v62, v[64:65], off
	s_nop 0
	global_load_dword v64, v[66:67], off
	v_lshl_add_u64 v[66:67], v[66:67], 0, s[20:21]
	v_lshl_add_u64 v[68:69], v[66:67], 0, s[20:21]
	v_lshl_add_u64 v[70:71], v[68:69], 0, s[20:21]
	v_lshl_add_u64 v[72:73], v[70:71], 0, s[20:21]
	global_load_dword v65, v[66:67], off
	s_nop 0
	global_load_dword v67, v[68:69], off
	s_nop 0
	global_load_dword v68, v[70:71], off
	s_nop 0
	global_load_dword v71, v[72:73], off
	v_lshl_add_u64 v[72:73], v[72:73], 0, s[20:21]
	global_load_dword v66, v[72:73], off
	v_lshl_add_u64 v[72:73], v[72:73], 0, s[20:21]
	global_load_dword v69, v[72:73], off
	v_lshl_add_u64 v[72:73], v[72:73], 0, s[20:21]
	v_lshl_add_u64 v[74:75], v[72:73], 0, s[20:21]
	global_load_dword v70, v[72:73], off
	s_nop 0
	global_load_dword v72, v[74:75], off
	v_lshl_add_u64 v[74:75], v[74:75], 0, s[20:21]
	v_lshl_add_u64 v[76:77], v[74:75], 0, s[20:21]
	s_waitcnt vmcnt(62)
; __device__ __forceinline__ void convert_item(Frame& F, int i0, LAS unsigned char* cvbuf) {
;     ...
;         for (int i = 0; i < 128; ++i) x[i] = c.src[(size_t)i * c.N];
;         if (c.f8) {
	v_lshl_add_u64 v[78:79], v[76:77], 0, s[20:21]
	v_lshl_add_u64 v[80:81], v[78:79], 0, s[20:21]
	global_load_dword v73, v[74:75], off
	s_nop 0
	global_load_dword v75, v[76:77], off
	s_nop 0
	global_load_dword v76, v[78:79], off
	s_nop 0
	global_load_dword v79, v[80:81], off
	v_lshl_add_u64 v[80:81], v[80:81], 0, s[20:21]
	global_load_dword v74, v[80:81], off
	v_lshl_add_u64 v[80:81], v[80:81], 0, s[20:21]
	global_load_dword v77, v[80:81], off
	v_lshl_add_u64 v[80:81], v[80:81], 0, s[20:21]
	v_lshl_add_u64 v[82:83], v[80:81], 0, s[20:21]
	global_load_dword v78, v[80:81], off
	s_nop 0
	global_load_dword v80, v[82:83], off
	v_lshl_add_u64 v[82:83], v[82:83], 0, s[20:21]
	v_lshl_add_u64 v[84:85], v[82:83], 0, s[20:21]
	v_lshl_add_u64 v[86:87], v[84:85], 0, s[20:21]
	v_lshl_add_u64 v[88:89], v[86:87], 0, s[20:21]
	global_load_dword v81, v[82:83], off
	s_nop 0
	global_load_dword v83, v[84:85], off
	s_nop 0
	global_load_dword v84, v[86:87], off
	s_nop 0
	global_load_dword v87, v[88:89], off
	v_lshl_add_u64 v[88:89], v[88:89], 0, s[20:21]
	global_load_dword v82, v[88:89], off
	v_lshl_add_u64 v[88:89], v[88:89], 0, s[20:21]
	global_load_dword v85, v[88:89], off
	v_lshl_add_u64 v[88:89], v[88:89], 0, s[20:21]
	v_lshl_add_u64 v[90:91], v[88:89], 0, s[20:21]
	global_load_dword v86, v[88:89], off
	s_nop 0
	global_load_dword v88, v[90:91], off
	v_lshl_add_u64 v[90:91], v[90:91], 0, s[20:21]
	v_lshl_add_u64 v[92:93], v[90:91], 0, s[20:21]
	v_lshl_add_u64 v[94:95], v[92:93], 0, s[20:21]
	v_lshl_add_u64 v[96:97], v[94:95], 0, s[20:21]
	global_load_dword v89, v[90:91], off
	s_nop 0
	global_load_dword v91, v[92:93], off
	s_nop 0
	global_load_dword v92, v[94:95], off
	s_nop 0
	global_load_dword v95, v[96:97], off
	v_lshl_add_u64 v[96:97], v[96:97], 0, s[20:21]
	global_load_dword v90, v[96:97], off
	v_lshl_add_u64 v[96:97], v[96:97], 0, s[20:21]
	global_load_dword v93, v[96:97], off
	v_lshl_add_u64 v[96:97], v[96:97], 0, s[20:21]
	v_lshl_add_u64 v[98:99], v[96:97], 0, s[20:21]
	global_load_dword v94, v[96:97], off
	s_nop 0
	global_load_dword v96, v[98:99], off
	v_lshl_add_u64 v[98:99], v[98:99], 0, s[20:21]
	v_lshl_add_u64 v[100:101], v[98:99], 0, s[20:21]
	v_lshl_add_u64 v[102:103], v[100:101], 0, s[20:21]
	v_lshl_add_u64 v[104:105], v[102:103], 0, s[20:21]
	global_load_dword v97, v[98:99], off
	s_nop 0
	global_load_dword v99, v[100:101], off
	s_nop 0
	global_load_dword v100, v[102:103], off
	s_nop 0
	global_load_dword v103, v[104:105], off
	v_lshl_add_u64 v[104:105], v[104:105], 0, s[20:21]
	global_load_dword v98, v[104:105], off
	v_lshl_add_u64 v[104:105], v[104:105], 0, s[20:21]
	global_load_dword v101, v[104:105], off
	v_lshl_add_u64 v[104:105], v[104:105], 0, s[20:21]
	v_lshl_add_u64 v[106:107], v[104:105], 0, s[20:21]
	global_load_dword v102, v[104:105], off
	s_nop 0
	global_load_dword v104, v[106:107], off
	v_lshl_add_u64 v[106:107], v[106:107], 0, s[20:21]
	v_lshl_add_u64 v[108:109], v[106:107], 0, s[20:21]
	v_lshl_add_u64 v[110:111], v[108:109], 0, s[20:21]
	v_lshl_add_u64 v[112:113], v[110:111], 0, s[20:21]
	global_load_dword v105, v[106:107], off
	s_nop 0
	global_load_dword v107, v[108:109], off
	s_nop 0
	global_load_dword v108, v[110:111], off
	s_nop 0
	global_load_dword v111, v[112:113], off
	v_lshl_add_u64 v[112:113], v[112:113], 0, s[20:21]
	global_load_dword v106, v[112:113], off
	v_lshl_add_u64 v[112:113], v[112:113], 0, s[20:21]
	global_load_dword v109, v[112:113], off
	v_lshl_add_u64 v[112:113], v[112:113], 0, s[20:21]
	v_lshl_add_u64 v[114:115], v[112:113], 0, s[20:21]
	global_load_dword v110, v[112:113], off
	s_nop 0
	global_load_dword v112, v[114:115], off
	v_lshl_add_u64 v[114:115], v[114:115], 0, s[20:21]
	v_lshl_add_u64 v[116:117], v[114:115], 0, s[20:21]
	v_lshl_add_u64 v[118:119], v[116:117], 0, s[20:21]
	v_lshl_add_u64 v[120:121], v[118:119], 0, s[20:21]
	global_load_dword v113, v[114:115], off
	s_nop 0
	global_load_dword v115, v[116:117], off
	s_nop 0
	global_load_dword v116, v[118:119], off
	s_nop 0
	global_load_dword v119, v[120:121], off
	v_lshl_add_u64 v[120:121], v[120:121], 0, s[20:21]
	global_load_dword v114, v[120:121], off
	v_lshl_add_u64 v[120:121], v[120:121], 0, s[20:21]
	global_load_dword v117, v[120:121], off
	v_lshl_add_u64 v[120:121], v[120:121], 0, s[20:21]
	v_lshl_add_u64 v[122:123], v[120:121], 0, s[20:21]
	global_load_dword v118, v[120:121], off
	s_nop 0
	global_load_dword v120, v[122:123], off
	v_lshl_add_u64 v[122:123], v[122:123], 0, s[20:21]
	v_lshl_add_u64 v[124:125], v[122:123], 0, s[20:21]
	v_lshl_add_u64 v[126:127], v[124:125], 0, s[20:21]
	v_lshl_add_u64 v[128:129], v[126:127], 0, s[20:21]
	global_load_dword v121, v[122:123], off
	s_nop 0
	global_load_dword v123, v[124:125], off
	s_nop 0
	global_load_dword v124, v[126:127], off
	s_nop 0
	global_load_dword v127, v[128:129], off
	v_lshl_add_u64 v[128:129], v[128:129], 0, s[20:21]
	global_load_dword v122, v[128:129], off
	v_lshl_add_u64 v[128:129], v[128:129], 0, s[20:21]
	global_load_dword v125, v[128:129], off
	v_lshl_add_u64 v[128:129], v[128:129], 0, s[20:21]
	v_lshl_add_u64 v[130:131], v[128:129], 0, s[20:21]
	global_load_dword v126, v[128:129], off
	s_nop 0
	global_load_dword v128, v[130:131], off
	v_lshl_add_u64 v[130:131], v[130:131], 0, s[20:21]
	v_lshl_add_u64 v[132:133], v[130:131], 0, s[20:21]
	v_lshl_add_u64 v[134:135], v[132:133], 0, s[20:21]
	v_lshl_add_u64 v[136:137], v[134:135], 0, s[20:21]
	global_load_dword v129, v[130:131], off
	s_nop 0
	global_load_dword v131, v[132:133], off
	s_nop 0
	global_load_dword v132, v[134:135], off
	s_nop 0
	global_load_dword v135, v[136:137], off
	v_lshl_add_u64 v[136:137], v[136:137], 0, s[20:21]
	global_load_dword v130, v[136:137], off
	v_lshl_add_u64 v[136:137], v[136:137], 0, s[20:21]
	global_load_dword v133, v[136:137], off
	v_lshl_add_u64 v[136:137], v[136:137], 0, s[20:21]
	s_waitcnt vmcnt(62)
	v_lshl_add_u64 v[138:139], v[136:137], 0, s[20:21]
	global_load_dword v134, v[136:137], off
	s_nop 0
	global_load_dword v136, v[138:139], off
	v_lshl_add_u64 v[138:139], v[138:139], 0, s[20:21]
	v_lshl_add_u64 v[140:141], v[138:139], 0, s[20:21]
	global_load_dword v137, v[138:139], off
	s_nop 0
	global_load_dword v138, v[140:141], off
	v_lshl_add_u64 v[140:141], v[140:141], 0, s[20:21]
	global_load_dword v139, v[140:141], off
	v_lshl_add_u64 v[140:141], v[140:141], 0, s[20:21]
	global_load_dword v140, v[140:141], off
	s_cbranch_vccz .LBB0_260
; #define LAS __attribute__((address_space(3)))
; __device__ __forceinline__ unsigned pk4f8(float a, float b, float c, float d) { int r = 0; r = __builtin_amdgcn_cvt_pk_fp8_f32(a, b, r, false); r = __builtin_amdgcn_cvt_pk_fp8_f32(c, d, r, true); return (unsigned)r; }
; __device__ __forceinline__ void convert_item(Frame& F, int i0, LAS unsigned char* cvbuf) {
;     ...
;         if (c.f8) {
;             const int lane = F.lane; LAS unsigned char* bw = cvbuf + lane * 144;
; #pragma unroll
;             for (int q = 0; q < 8; ++q) { v4u o; o.x = pk4f8(x[16 * q + 0] * F8_SW, x[16 * q + 1] * F8_SW, x[16 * q + 2] * F8_SW, x[16 * q + 3] * F8_SW); o.y = pk4f8(x[16 * q + 4] * F8_SW, x[16 * q + 5] * F8_SW, x[16 * q + 6] * F8_SW, x[16 * q + 7] * F8_SW);
;                 o.z = pk4f8(x[16 * q + 8] * F8_SW, x[16 * q + 9] * F8_SW, x[16 * q + 10] * F8_SW, x[16 * q + 11] * F8_SW); o.w = pk4f8(x[16 * q + 12] * F8_SW, x[16 * q + 13] * F8_SW, x[16 * q + 14] * F8_SW, x[16 * q + 15] * F8_SW);
;                 *(LAS v4u*)(bw + 16 * q) = o; }
	s_waitcnt vmcnt(62)
	v_mul_f32_e32 v141, 0x43800000, v15
	v_mul_f32_e32 v143, 0x43800000, v13
	v_mov_b32_e32 v142, v3
	v_cvt_pk_fp8_f32 v142, v141, v143
	v_mul_f32_e32 v141, 0x43800000, v18
	v_mul_f32_e32 v146, 0x43800000, v19
	v_mov_b32_e32 v143, v3
	v_cvt_pk_fp8_f32 v143, v141, v146
	v_mul_f32_e32 v144, 0x43800000, v16
	v_mul_f32_e32 v145, 0x43800000, v17
	v_cvt_pk_fp8_f32 v142, v144, v145 op_sel:[0,0,1]
	v_mul_f32_e32 v141, 0x43800000, v20
	v_mul_f32_e32 v144, 0x43800000, v23
	v_cvt_pk_fp8_f32 v143, v141, v144 op_sel:[0,0,1]
	v_mul_f32_e32 v141, 0x43800000, v12
	v_mul_f32_e32 v145, 0x43800000, v21
	v_mov_b32_e32 v144, v3
	v_cvt_pk_fp8_f32 v144, v141, v145
	v_mul_f32_e32 v141, 0x43800000, v25
	v_mul_f32_e32 v148, 0x43800000, v27
	v_mov_b32_e32 v145, v3
	v_cvt_pk_fp8_f32 v145, v141, v148
	v_mul_f32_e32 v146, 0x43800000, v22
	v_mul_f32_e32 v147, 0x43800000, v24
	v_cvt_pk_fp8_f32 v144, v146, v147 op_sel:[0,0,1]
	v_mul_f32_e32 v141, 0x43800000, v28
	v_mul_f32_e32 v146, 0x43800000, v31
	v_cvt_pk_fp8_f32 v145, v141, v146 op_sel:[0,0,1]
	v_mul_f32_e32 v141, 0x43800000, v26
	v_mul_f32_e32 v147, 0x43800000, v29
	v_mov_b32_e32 v146, v3
	v_cvt_pk_fp8_f32 v146, v141, v147
	v_mul_f32_e32 v141, 0x43800000, v33
	v_mul_f32_e32 v150, 0x43800000, v35
	v_mov_b32_e32 v147, v3
	v_cvt_pk_fp8_f32 v147, v141, v150
	v_mul_f32_e32 v148, 0x43800000, v30
	v_mul_f32_e32 v149, 0x43800000, v32
	v_cvt_pk_fp8_f32 v146, v148, v149 op_sel:[0,0,1]
	v_mul_f32_e32 v141, 0x43800000, v36
	v_mul_f32_e32 v148, 0x43800000, v39
	v_cvt_pk_fp8_f32 v147, v141, v148 op_sel:[0,0,1]
	v_mul_f32_e32 v141, 0x43800000, v34
	v_mul_f32_e32 v149, 0x43800000, v37
	v_mov_b32_e32 v148, v3
	v_cvt_pk_fp8_f32 v148, v141, v149
	v_mul_f32_e32 v141, 0x43800000, v41
	v_mul_f32_e32 v152, 0x43800000, v43
	v_mov_b32_e32 v149, v3
	v_cvt_pk_fp8_f32 v149, v141, v152
	v_mul_f32_e32 v150, 0x43800000, v38
	v_mul_f32_e32 v151, 0x43800000, v40
	v_cvt_pk_fp8_f32 v148, v150, v151 op_sel:[0,0,1]
	v_mul_f32_e32 v141, 0x43800000, v44
	v_mul_f32_e32 v150, 0x43800000, v47
	v_cvt_pk_fp8_f32 v149, v141, v150 op_sel:[0,0,1]
	v_mul_f32_e32 v141, 0x43800000, v42
	v_mul_f32_e32 v151, 0x43800000, v45
	v_mov_b32_e32 v150, v3
	v_cvt_pk_fp8_f32 v150, v141, v151
	v_mul_f32_e32 v141, 0x43800000, v49
	v_mul_f32_e32 v154, 0x43800000, v51
	v_mov_b32_e32 v151, v3
	v_cvt_pk_fp8_f32 v151, v141, v154
	v_mul_f32_e32 v152, 0x43800000, v46
	v_mul_f32_e32 v153, 0x43800000, v48
	v_cvt_pk_fp8_f32 v150, v152, v153 op_sel:[0,0,1]
	v_mul_f32_e32 v141, 0x43800000, v52
	v_mul_f32_e32 v152, 0x43800000, v55
	v_cvt_pk_fp8_f32 v151, v141, v152 op_sel:[0,0,1]
	v_mul_f32_e32 v141, 0x43800000, v50
	v_mul_f32_e32 v153, 0x43800000, v53
	v_mov_b32_e32 v152, v3
	v_cvt_pk_fp8_f32 v152, v141, v153
	v_mul_f32_e32 v141, 0x43800000, v57
	v_mul_f32_e32 v156, 0x43800000, v59
	v_mov_b32_e32 v153, v3
	v_cvt_pk_fp8_f32 v153, v141, v156
	v_mul_f32_e32 v154, 0x43800000, v54
	v_mul_f32_e32 v155, 0x43800000, v56
	v_cvt_pk_fp8_f32 v152, v154, v155 op_sel:[0,0,1]
	v_mul_f32_e32 v141, 0x43800000, v60
	v_mul_f32_e32 v154, 0x43800000, v63
	v_cvt_pk_fp8_f32 v153, v141, v154 op_sel:[0,0,1]
	v_mul_f32_e32 v141, 0x43800000, v58
	v_mul_f32_e32 v155, 0x43800000, v61
	v_mov_b32_e32 v154, v3
	v_cvt_pk_fp8_f32 v154, v141, v155
	v_mul_f32_e32 v141, 0x43800000, v65
	v_mul_f32_e32 v158, 0x43800000, v67
	v_mov_b32_e32 v155, v3
	v_cvt_pk_fp8_f32 v155, v141, v158
	v_mul_f32_e32 v156, 0x43800000, v62
	v_mul_f32_e32 v157, 0x43800000, v64
	v_cvt_pk_fp8_f32 v154, v156, v157 op_sel:[0,0,1]
	v_mul_f32_e32 v141, 0x43800000, v68
	v_mul_f32_e32 v156, 0x43800000, v71
	v_cvt_pk_fp8_f32 v155, v141, v156 op_sel:[0,0,1]
	v_mul_f32_e32 v141, 0x43800000, v66
	v_mul_f32_e32 v157, 0x43800000, v69
	v_mov_b32_e32 v156, v3
	v_cvt_pk_fp8_f32 v156, v141, v157
	v_mul_f32_e32 v141, 0x43800000, v73
	v_mul_f32_e32 v160, 0x43800000, v75
	v_mov_b32_e32 v157, v3
	v_cvt_pk_fp8_f32 v157, v141, v160
	v_mul_f32_e32 v158, 0x43800000, v70
	v_mul_f32_e32 v159, 0x43800000, v72
	v_cvt_pk_fp8_f32 v156, v158, v159 op_sel:[0,0,1]
	v_mul_f32_e32 v141, 0x43800000, v76
	v_mul_f32_e32 v158, 0x43800000, v79
	v_cvt_pk_fp8_f32 v157, v141, v158 op_sel:[0,0,1]
	ds_write_b128 v1, v[142:145]
	ds_write_b128 v1, v[146:149] offset:16
	ds_write_b128 v1, v[150:153] offset:32
	ds_write_b128 v1, v[154:157] offset:48
	v_mul_f32_e32 v141, 0x43800000, v74
	v_mul_f32_e32 v143, 0x43800000, v77
	v_mov_b32_e32 v142, v3
	v_cvt_pk_fp8_f32 v142, v141, v143
	s_waitcnt vmcnt(59)
	v_mul_f32_e32 v141, 0x43800000, v81
	s_waitcnt vmcnt(58)
	v_mul_f32_e32 v146, 0x43800000, v83
	v_mov_b32_e32 v143, v3
	v_cvt_pk_fp8_f32 v143, v141, v146
	v_mul_f32_e32 v144, 0x43800000, v78
	v_mul_f32_e32 v145, 0x43800000, v80
	v_cvt_pk_fp8_f32 v142, v144, v145 op_sel:[0,0,1]
	s_waitcnt vmcnt(57)
	v_mul_f32_e32 v141, 0x43800000, v84
	s_waitcnt vmcnt(56)
	v_mul_f32_e32 v144, 0x43800000, v87
	v_cvt_pk_fp8_f32 v143, v141, v144 op_sel:[0,0,1]
	s_waitcnt vmcnt(55)
	v_mul_f32_e32 v141, 0x43800000, v82
	s_waitcnt vmcnt(54)
	v_mul_f32_e32 v145, 0x43800000, v85
	v_mov_b32_e32 v144, v3
	v_cvt_pk_fp8_f32 v144, v141, v145
	s_waitcnt vmcnt(51)
	v_mul_f32_e32 v141, 0x43800000, v89
	s_waitcnt vmcnt(50)
	v_mul_f32_e32 v148, 0x43800000, v91
	v_mov_b32_e32 v145, v3
	v_cvt_pk_fp8_f32 v145, v141, v148
	v_mul_f32_e32 v146, 0x43800000, v86
	v_mul_f32_e32 v147, 0x43800000, v88
	v_cvt_pk_fp8_f32 v144, v146, v147 op_sel:[0,0,1]
	s_waitcnt vmcnt(49)
	v_mul_f32_e32 v141, 0x43800000, v92
	s_waitcnt vmcnt(48)
	v_mul_f32_e32 v146, 0x43800000, v95
	v_cvt_pk_fp8_f32 v145, v141, v146 op_sel:[0,0,1]
	s_waitcnt vmcnt(47)
	v_mul_f32_e32 v141, 0x43800000, v90
	s_waitcnt vmcnt(46)
; #define LAS __attribute__((address_space(3)))
; __device__ __forceinline__ unsigned pk4f8(float a, float b, float c, float d) { int r = 0; r = __builtin_amdgcn_cvt_pk_fp8_f32(a, b, r, false); r = __builtin_amdgcn_cvt_pk_fp8_f32(c, d, r, true); return (unsigned)r; }
; __device__ __forceinline__ void convert_item(Frame& F, int i0, LAS unsigned char* cvbuf) {
;     ...
;             for (int q = 0; q < 8; ++q) { v4u o; o.x = pk4f8(x[16 * q + 0] * F8_SW, x[16 * q + 1] * F8_SW, x[16 * q + 2] * F8_SW, x[16 * q + 3] * F8_SW); o.y = pk4f8(x[16 * q + 4] * F8_SW, x[16 * q + 5] * F8_SW, x[16 * q + 6] * F8_SW, x[16 * q + 7] * F8_SW);
;                 o.z = pk4f8(x[16 * q + 8] * F8_SW, x[16 * q + 9] * F8_SW, x[16 * q + 10] * F8_SW, x[16 * q + 11] * F8_SW); o.w = pk4f8(x[16 * q + 12] * F8_SW, x[16 * q + 13] * F8_SW, x[16 * q + 14] * F8_SW, x[16 * q + 15] * F8_SW);
;                 *(LAS v4u*)(bw + 16 * q) = o; }
;             unsigned char* d0 = c.dst - (size_t)lane * 2048 + (size_t)(lane >> 3) * 2048 + (lane & 7) * 16; const LAS unsigned char* br = cvbuf + (lane >> 3) * 144 + (lane & 7) * 16;
; #pragma unroll
;             for (int i = 0; i < 8; ++i) { const v4u v = *(const LAS v4u*)(br + i * 8 * 144); *(v4u*)(d0 + (size_t)i * 8 * 2048) = v; } }
	v_mul_f32_e32 v147, 0x43800000, v93
	v_mov_b32_e32 v146, v3
	v_cvt_pk_fp8_f32 v146, v141, v147
	s_waitcnt vmcnt(43)
	v_mul_f32_e32 v141, 0x43800000, v97
	s_waitcnt vmcnt(42)
	v_mul_f32_e32 v150, 0x43800000, v99
	v_mov_b32_e32 v147, v3
	v_cvt_pk_fp8_f32 v147, v141, v150
	v_mul_f32_e32 v148, 0x43800000, v94
	v_mul_f32_e32 v149, 0x43800000, v96
	v_cvt_pk_fp8_f32 v146, v148, v149 op_sel:[0,0,1]
	s_waitcnt vmcnt(41)
	v_mul_f32_e32 v141, 0x43800000, v100
	s_waitcnt vmcnt(40)
	v_mul_f32_e32 v148, 0x43800000, v103
	v_cvt_pk_fp8_f32 v147, v141, v148 op_sel:[0,0,1]
	s_waitcnt vmcnt(39)
	v_mul_f32_e32 v141, 0x43800000, v98
	s_waitcnt vmcnt(38)
	v_mul_f32_e32 v149, 0x43800000, v101
	v_mov_b32_e32 v148, v3
	v_cvt_pk_fp8_f32 v148, v141, v149
	s_waitcnt vmcnt(35)
	v_mul_f32_e32 v141, 0x43800000, v105
	s_waitcnt vmcnt(34)
	v_mul_f32_e32 v152, 0x43800000, v107
	v_mov_b32_e32 v149, v3
	v_cvt_pk_fp8_f32 v149, v141, v152
	v_mul_f32_e32 v150, 0x43800000, v102
	v_mul_f32_e32 v151, 0x43800000, v104
	v_cvt_pk_fp8_f32 v148, v150, v151 op_sel:[0,0,1]
	s_waitcnt vmcnt(33)
	v_mul_f32_e32 v141, 0x43800000, v108
	s_waitcnt vmcnt(32)
	v_mul_f32_e32 v150, 0x43800000, v111
	v_cvt_pk_fp8_f32 v149, v141, v150 op_sel:[0,0,1]
	s_waitcnt vmcnt(31)
	v_mul_f32_e32 v141, 0x43800000, v106
	s_waitcnt vmcnt(30)
	v_mul_f32_e32 v151, 0x43800000, v109
	v_mov_b32_e32 v150, v3
	v_cvt_pk_fp8_f32 v150, v141, v151
	s_waitcnt vmcnt(27)
	v_mul_f32_e32 v141, 0x43800000, v113
	s_waitcnt vmcnt(26)
	v_mul_f32_e32 v154, 0x43800000, v115
	v_mov_b32_e32 v151, v3
	v_cvt_pk_fp8_f32 v151, v141, v154
	v_mul_f32_e32 v152, 0x43800000, v110
	v_mul_f32_e32 v153, 0x43800000, v112
	v_cvt_pk_fp8_f32 v150, v152, v153 op_sel:[0,0,1]
	s_waitcnt vmcnt(25)
	v_mul_f32_e32 v141, 0x43800000, v116
	s_waitcnt vmcnt(24)
	v_mul_f32_e32 v152, 0x43800000, v119
	v_cvt_pk_fp8_f32 v151, v141, v152 op_sel:[0,0,1]
	s_waitcnt vmcnt(23)
	v_mul_f32_e32 v141, 0x43800000, v114
	s_waitcnt vmcnt(22)
	v_mul_f32_e32 v153, 0x43800000, v117
	v_mov_b32_e32 v152, v3
	v_cvt_pk_fp8_f32 v152, v141, v153
	s_waitcnt vmcnt(19)
	v_mul_f32_e32 v141, 0x43800000, v121
	s_waitcnt vmcnt(18)
	v_mul_f32_e32 v156, 0x43800000, v123
	v_mov_b32_e32 v153, v3
	v_cvt_pk_fp8_f32 v153, v141, v156
	v_mul_f32_e32 v154, 0x43800000, v118
	v_mul_f32_e32 v155, 0x43800000, v120
	v_cvt_pk_fp8_f32 v152, v154, v155 op_sel:[0,0,1]
	s_waitcnt vmcnt(17)
	v_mul_f32_e32 v141, 0x43800000, v124
	s_waitcnt vmcnt(16)
	v_mul_f32_e32 v154, 0x43800000, v127
	v_cvt_pk_fp8_f32 v153, v141, v154 op_sel:[0,0,1]
	s_waitcnt vmcnt(15)
	v_mul_f32_e32 v141, 0x43800000, v122
	s_waitcnt vmcnt(14)
	v_mul_f32_e32 v155, 0x43800000, v125
	v_mov_b32_e32 v154, v3
	v_cvt_pk_fp8_f32 v154, v141, v155
	s_waitcnt vmcnt(11)
	v_mul_f32_e32 v141, 0x43800000, v129
	s_waitcnt vmcnt(10)
	v_mul_f32_e32 v158, 0x43800000, v131
	v_mov_b32_e32 v155, v3
	v_cvt_pk_fp8_f32 v155, v141, v158
	v_mul_f32_e32 v156, 0x43800000, v126
	v_mul_f32_e32 v157, 0x43800000, v128
	v_cvt_pk_fp8_f32 v154, v156, v157 op_sel:[0,0,1]
	s_waitcnt vmcnt(9)
	v_mul_f32_e32 v141, 0x43800000, v132
	s_waitcnt vmcnt(8)
	v_mul_f32_e32 v156, 0x43800000, v135
	v_cvt_pk_fp8_f32 v155, v141, v156 op_sel:[0,0,1]
	s_waitcnt vmcnt(7)
	v_mul_f32_e32 v141, 0x43800000, v130
	s_waitcnt vmcnt(6)
	v_mul_f32_e32 v157, 0x43800000, v133
	v_mov_b32_e32 v156, v3
	v_cvt_pk_fp8_f32 v156, v141, v157
	s_waitcnt vmcnt(3)
	v_mul_f32_e32 v141, 0x43800000, v137
	s_waitcnt vmcnt(2)
	v_mul_f32_e32 v160, 0x43800000, v138
	v_mov_b32_e32 v157, v3
	v_cvt_pk_fp8_f32 v157, v141, v160
	v_mul_f32_e32 v158, 0x43800000, v134
	v_mul_f32_e32 v159, 0x43800000, v136
	v_cvt_pk_fp8_f32 v156, v158, v159 op_sel:[0,0,1]
	s_waitcnt vmcnt(1)
	v_mul_f32_e32 v141, 0x43800000, v139
	s_waitcnt vmcnt(0)
	v_mul_f32_e32 v158, 0x43800000, v140
	v_cvt_pk_fp8_f32 v157, v141, v158 op_sel:[0,0,1]
	ds_write_b128 v1, v[142:145] offset:64
	ds_write_b128 v1, v[146:149] offset:80
	ds_write_b128 v1, v[150:153] offset:96
	ds_write_b128 v1, v[154:157] offset:112
	ds_read_b128 v[142:145], v14
	v_lshl_add_u64 v[146:147], v[10:11], 0, v[4:5]
	v_lshl_add_u64 v[146:147], v[146:147], 0, v[6:7]
	v_lshl_add_u64 v[150:151], v[146:147], 0, v[8:9]
	ds_read_b128 v[146:149], v14 offset:1152
	s_movk_i32 s8, 0x4000
	s_waitcnt lgkmcnt(1)
	global_store_dwordx4 v[150:151], v[142:145], off nt
	s_mov_b64 s[18:19], 0
	s_nop 0
	v_add_co_u32_e32 v142, vcc, s8, v150
	s_nop 1
	v_addc_co_u32_e32 v143, vcc, 0, v151, vcc
	s_waitcnt lgkmcnt(0)
	global_store_dwordx4 v[142:143], v[146:149], off nt
	ds_read_b128 v[142:145], v14 offset:2304
	ds_read_b128 v[146:149], v14 offset:3456
	v_add_co_u32_e32 v152, vcc, s28, v150
	s_nop 1
	v_addc_co_u32_e32 v153, vcc, 0, v151, vcc
	s_waitcnt lgkmcnt(1)
	global_store_dwordx4 v[152:153], v[142:145], off nt
	s_nop 1
	v_add_co_u32_e32 v142, vcc, s29, v150
	s_nop 1
	v_addc_co_u32_e32 v143, vcc, 0, v151, vcc
	s_waitcnt lgkmcnt(0)
	global_store_dwordx4 v[142:143], v[146:149], off nt
	ds_read_b128 v[142:145], v14 offset:4608
	ds_read_b128 v[146:149], v14 offset:5760
	v_add_co_u32_e32 v152, vcc, s30, v150
	s_nop 1
	v_addc_co_u32_e32 v153, vcc, 0, v151, vcc
	s_waitcnt lgkmcnt(1)
	global_store_dwordx4 v[152:153], v[142:145], off nt
	s_nop 1
	v_add_co_u32_e32 v142, vcc, 0x14000, v150
	s_nop 1
	v_addc_co_u32_e32 v143, vcc, 0, v151, vcc
	s_waitcnt lgkmcnt(0)
	global_store_dwordx4 v[142:143], v[146:149], off nt
	ds_read_b128 v[142:145], v14 offset:6912
	ds_read_b128 v[146:149], v14 offset:8064
	v_add_co_u32_e32 v152, vcc, 0x18000, v150
	s_nop 1
	v_addc_co_u32_e32 v153, vcc, 0, v151, vcc
	s_waitcnt lgkmcnt(1)
	global_store_dwordx4 v[152:153], v[142:145], off nt
	s_nop 1
	v_add_co_u32_e32 v142, vcc, 0x1c000, v150
	s_nop 1
	v_addc_co_u32_e32 v143, vcc, 0, v151, vcc
	s_waitcnt lgkmcnt(0)
	global_store_dwordx4 v[142:143], v[146:149], off nt
; __device__ __forceinline__ unsigned pk2(float lo, float hi) { const f32x2 v = {lo, hi}; const bf16x2_t b = __builtin_convertvector(v, bf16x2_t); return __builtin_bit_cast(unsigned, b); }
; __device__ __forceinline__ void convert_item(Frame& F, int i0, LAS unsigned char* cvbuf) {
;     ...
;         else {
; #pragma unroll
;             for (int q = 0; q < 16; ++q) { v4u o; o.x = pk2(x[8 * q + 0], x[8 * q + 1]); o.y = pk2(x[8 * q + 2], x[8 * q + 3]); o.z = pk2(x[8 * q + 4], x[8 * q + 5]); o.w = pk2(x[8 * q + 6], x[8 * q + 7]);
;                 *(v4u*)(c.dst + 16 * q) = o; } } }
.LBB0_260:
	s_andn2_b64 vcc, exec, s[18:19]
	s_cbranch_vccnz .LBB0_237
	s_waitcnt vmcnt(62)
	v_cvt_pk_bf16_f32 v143, v16, v17
	v_cvt_pk_bf16_f32 v144, v18, v19
	v_cvt_pk_bf16_f32 v16, v12, v21
	v_cvt_pk_bf16_f32 v17, v22, v24
	v_cvt_pk_bf16_f32 v18, v25, v27
	v_cvt_pk_bf16_f32 v19, v28, v31
	global_store_dwordx4 v[10:11], v[16:19], off offset:16 nt
	v_cvt_pk_bf16_f32 v142, v15, v13
	v_cvt_pk_bf16_f32 v145, v20, v23
	v_cvt_pk_bf16_f32 v16, v26, v29
	v_cvt_pk_bf16_f32 v17, v30, v32
	v_cvt_pk_bf16_f32 v18, v33, v35
	v_cvt_pk_bf16_f32 v19, v36, v39
	global_store_dwordx4 v[10:11], v[16:19], off offset:32 nt
	global_store_dwordx4 v[10:11], v[142:145], off nt
	s_nop 0
	v_cvt_pk_bf16_f32 v16, v34, v37
	v_cvt_pk_bf16_f32 v17, v38, v40
	v_cvt_pk_bf16_f32 v18, v41, v43
	v_cvt_pk_bf16_f32 v19, v44, v47
	global_store_dwordx4 v[10:11], v[16:19], off offset:48 nt
	s_nop 1
	v_cvt_pk_bf16_f32 v16, v42, v45
	v_cvt_pk_bf16_f32 v17, v46, v48
	v_cvt_pk_bf16_f32 v18, v49, v51
	v_cvt_pk_bf16_f32 v19, v52, v55
	global_store_dwordx4 v[10:11], v[16:19], off offset:64 nt
	s_nop 1
	v_cvt_pk_bf16_f32 v16, v50, v53
	v_cvt_pk_bf16_f32 v17, v54, v56
	v_cvt_pk_bf16_f32 v18, v57, v59
	v_cvt_pk_bf16_f32 v19, v60, v63
	global_store_dwordx4 v[10:11], v[16:19], off offset:80 nt
	s_nop 1
	v_cvt_pk_bf16_f32 v16, v58, v61
	v_cvt_pk_bf16_f32 v17, v62, v64
	v_cvt_pk_bf16_f32 v18, v65, v67
	v_cvt_pk_bf16_f32 v19, v68, v71
	global_store_dwordx4 v[10:11], v[16:19], off offset:96 nt
	s_nop 1
	v_cvt_pk_bf16_f32 v16, v66, v69
	v_cvt_pk_bf16_f32 v17, v70, v72
	v_cvt_pk_bf16_f32 v18, v73, v75
	v_cvt_pk_bf16_f32 v19, v76, v79
	global_store_dwordx4 v[10:11], v[16:19], off offset:112 nt
	s_nop 1
	v_cvt_pk_bf16_f32 v16, v74, v77
	s_waitcnt vmcnt(62)
	v_cvt_pk_bf16_f32 v17, v78, v80
	v_cvt_pk_bf16_f32 v18, v81, v83
	v_cvt_pk_bf16_f32 v19, v84, v87
	global_store_dwordx4 v[10:11], v[16:19], off offset:128 nt
	s_nop 1
	v_cvt_pk_bf16_f32 v16, v82, v85
	s_waitcnt vmcnt(61)
	v_cvt_pk_bf16_f32 v17, v86, v88
	s_waitcnt vmcnt(59)
	v_cvt_pk_bf16_f32 v18, v89, v91
	s_waitcnt vmcnt(57)
	v_cvt_pk_bf16_f32 v19, v92, v95
	global_store_dwordx4 v[10:11], v[16:19], off offset:144 nt
	s_waitcnt vmcnt(56)
	s_nop 0
	v_cvt_pk_bf16_f32 v16, v90, v93
	s_waitcnt vmcnt(54)
	v_cvt_pk_bf16_f32 v17, v94, v96
	s_waitcnt vmcnt(52)
	v_cvt_pk_bf16_f32 v18, v97, v99
	s_waitcnt vmcnt(50)
	v_cvt_pk_bf16_f32 v19, v100, v103
	global_store_dwordx4 v[10:11], v[16:19], off offset:160 nt
	s_waitcnt vmcnt(49)
	s_nop 0
	v_cvt_pk_bf16_f32 v16, v98, v101
	s_waitcnt vmcnt(47)
	v_cvt_pk_bf16_f32 v17, v102, v104
	s_waitcnt vmcnt(45)
	v_cvt_pk_bf16_f32 v18, v105, v107
	s_waitcnt vmcnt(43)
	v_cvt_pk_bf16_f32 v19, v108, v111
	global_store_dwordx4 v[10:11], v[16:19], off offset:176 nt
	s_waitcnt vmcnt(42)
	s_nop 0
	v_cvt_pk_bf16_f32 v16, v106, v109
	s_waitcnt vmcnt(40)
	v_cvt_pk_bf16_f32 v17, v110, v112
	s_waitcnt vmcnt(38)
	v_cvt_pk_bf16_f32 v18, v113, v115
	s_waitcnt vmcnt(36)
	v_cvt_pk_bf16_f32 v19, v116, v119
	global_store_dwordx4 v[10:11], v[16:19], off offset:192 nt
	s_waitcnt vmcnt(35)
	s_nop 0
	v_cvt_pk_bf16_f32 v16, v114, v117
	s_waitcnt vmcnt(33)
	v_cvt_pk_bf16_f32 v17, v118, v120
	s_waitcnt vmcnt(31)
	v_cvt_pk_bf16_f32 v18, v121, v123
	s_waitcnt vmcnt(29)
	v_cvt_pk_bf16_f32 v19, v124, v127
	global_store_dwordx4 v[10:11], v[16:19], off offset:208 nt
	s_waitcnt vmcnt(28)
	s_nop 0
	v_cvt_pk_bf16_f32 v16, v122, v125
	s_waitcnt vmcnt(26)
	v_cvt_pk_bf16_f32 v17, v126, v128
	s_waitcnt vmcnt(24)
	v_cvt_pk_bf16_f32 v18, v129, v131
	s_waitcnt vmcnt(22)
	v_cvt_pk_bf16_f32 v19, v132, v135
	global_store_dwordx4 v[10:11], v[16:19], off offset:224 nt
	s_waitcnt vmcnt(21)
	s_nop 0
	v_cvt_pk_bf16_f32 v16, v130, v133
	s_waitcnt vmcnt(19)
	v_cvt_pk_bf16_f32 v17, v134, v136
	s_waitcnt vmcnt(17)
	v_cvt_pk_bf16_f32 v18, v137, v138
	s_waitcnt vmcnt(15)
	v_cvt_pk_bf16_f32 v19, v139, v140
	global_store_dwordx4 v[10:11], v[16:19], off offset:240 nt
	s_branch .LBB0_237
